# pre-PEER norm phase (norm2) rewritten by hand too (two rows in flight, DPP wave sum, 16-byte stores)
# baseline (speedup 1.0000x reference)
.LBB0_762:
	s_andn2_b64 vcc, exec, s[6:7]
	s_cbranch_vccnz .LBB0_834
	v_readfirstlane_b32 s16, v0
	s_lshr_b32 s16, s16, 6
	s_lshl_b32 s17, s2, 3
	s_add_u32 s16, s16, s17
	s_lshl_b32 s17, s82, 3
	s_add_u32 s18, s96, s17
	s_sub_u32 s18, s18, 1
	v_cvt_f32_u32_e32 v136, s17
	v_cvt_f32_u32_e32 v137, s18
	v_rcp_iflag_f32_e32 v136, v136
	s_nop 0
	v_mul_f32_e32 v136, v137, v136
	v_cvt_u32_f32_e32 v136, v136
	s_nop 0
	v_readfirstlane_b32 s19, v136
	s_mul_i32 s12, s19, s17
	s_cmp_gt_u32 s12, s18
	s_cselect_b32 s13, 1, 0
	s_sub_u32 s19, s19, s13
	s_add_u32 s12, s19, 1
	s_mul_i32 s12, s12, s17
	s_cmp_le_u32 s12, s18
	s_cselect_b32 s13, 1, 0
	s_add_u32 s19, s19, s13
	s_mul_i32 s12, s16, s19
	s_cmp_ge_u32 s12, s96
	s_cbranch_scc1 .Lpq_end
	s_add_u32 s13, s12, s19
	s_min_u32 s13, s13, s96
	v_readlane_b32 s4, v252, 4
	v_readlane_b32 s5, v252, 5
	v_readlane_b32 s14, v255, 34
	s_sub_u32 s4, s4, 0x18
	s_subb_u32 s5, s5, 0
	s_load_dwordx2 s[4:5], s[4:5], 0x0
	v_and_b32_e32 v2, 63, v0
	v_lshlrev_b32_e32 v3, 4, v2
	v_lshlrev_b32_e32 v160, 5, v2
	v_add_u32_e32 v161, 0x1000, v160
	s_mul_i32 s16, s14, 0x3c000
	s_mul_i32 s17, s14, 0xc000
	s_lshl_b32 s18, s14, 13
	v_readlane_b32 s48, v252, 16
	v_readlane_b32 s49, v252, 17
	v_readlane_b32 s50, v252, 20
	v_readlane_b32 s51, v252, 21
	s_waitcnt lgkmcnt(0)
	s_add_u32 s38, s4, 0x15000000
	s_addc_u32 s39, s5, 0
	s_add_u32 s42, s4, 0x1b200000
	s_addc_u32 s43, s5, 0
	s_add_u32 s46, s4, 0x10000
	s_addc_u32 s47, s5, 0
	s_add_u32 s46, s46, s16
	s_addc_u32 s47, s47, 0
	s_add_u32 s48, s48, s17
	s_addc_u32 s49, s49, 0
	s_add_u32 s50, s50, s18
	s_addc_u32 s51, s51, 0
	s_mov_b32 s15, -1
	s_lshl_b32 s16, s12, 12
	s_add_u32 s52, s38, s16
	s_addc_u32 s53, s39, 0
	global_load_dwordx4 v[102:105], v3, s[52:53]
	global_load_dwordx4 v[106:109], v3, s[52:53] offset:1024
	global_load_dwordx4 v[110:113], v3, s[52:53] offset:2048
	global_load_dwordx4 v[114:117], v3, s[52:53] offset:3072
	s_add_u32 s18, s12, 1
	s_sub_u32 s19, s13, 1
	s_min_u32 s18, s18, s19
	s_lshl_b32 s16, s18, 12
	s_add_u32 s52, s38, s16
	s_addc_u32 s53, s39, 0
	global_load_dwordx4 v[118:121], v3, s[52:53]
	global_load_dwordx4 v[122:125], v3, s[52:53] offset:1024
	global_load_dwordx4 v[126:129], v3, s[52:53] offset:2048
	global_load_dwordx4 v[130:133], v3, s[52:53] offset:3072
	s_lshr_b32 s16, s12, 12
	s_cmp_lt_u32 s12, 0x4000
	s_cselect_b32 s16, s16, 4
	s_cmp_eq_u32 s16, s15
	s_cbranch_scc1 .Lpq_mod_ok_a
	s_mov_b32 s15, s16
	s_mul_i32 s16, s16, 0xc000
	s_add_u32 s52, s46, s16
	s_addc_u32 s53, s47, 0
	s_add_u32 s10, s52, 0x8000
	s_addc_u32 s11, s53, 0
	s_add_u32 s52, s52, 0x6000
	s_addc_u32 s53, s53, 0
	s_add_u32 s16, s48, 0x8000
	s_addc_u32 s17, s49, 0
	s_add_u32 s18, s48, 0x6000
	s_addc_u32 s19, s49, 0
	global_load_dwordx4 v[6:9], v160, s[10:11]
	global_load_dwordx4 v[70:73], v160, s[16:17]
	global_load_dwordx4 v[38:41], v160, s[52:53]
	global_load_dwordx4 v[10:13], v160, s[10:11] offset:16
	global_load_dwordx4 v[74:77], v160, s[16:17] offset:16
	global_load_dwordx4 v[42:45], v160, s[52:53] offset:16
	global_load_dwordx4 v[14:17], v160, s[10:11] offset:2048
	global_load_dwordx4 v[78:81], v160, s[16:17] offset:2048
	global_load_dwordx4 v[46:49], v160, s[52:53] offset:2048
	global_load_dwordx4 v[18:21], v160, s[10:11] offset:2064
	global_load_dwordx4 v[82:85], v160, s[16:17] offset:2064
	global_load_dwordx4 v[50:53], v160, s[52:53] offset:2064
	global_load_dwordx4 v[22:25], v161, s[10:11]
	global_load_dwordx4 v[86:89], v161, s[16:17]
	global_load_dwordx4 v[54:57], v161, s[52:53]
	global_load_dwordx4 v[26:29], v161, s[10:11] offset:16
	global_load_dwordx4 v[90:93], v161, s[16:17] offset:16
	global_load_dwordx4 v[58:61], v161, s[52:53] offset:16
	global_load_dwordx4 v[30:33], v161, s[10:11] offset:2048
	global_load_dwordx4 v[94:97], v161, s[16:17] offset:2048
	global_load_dwordx4 v[62:65], v161, s[52:53] offset:2048
	global_load_dwordx4 v[34:37], v161, s[10:11] offset:2064
	global_load_dwordx4 v[98:101], v161, s[16:17] offset:2064
	global_load_dwordx4 v[66:69], v161, s[52:53] offset:2064
	s_waitcnt vmcnt(0)
	v_pk_add_f32 v[6:7], v[6:7], v[70:71]
	v_pk_add_f32 v[6:7], v[6:7], 1.0 op_sel_hi:[1,0]
	v_pk_add_f32 v[8:9], v[8:9], v[72:73]
	v_pk_add_f32 v[8:9], v[8:9], 1.0 op_sel_hi:[1,0]
	v_pk_add_f32 v[10:11], v[10:11], v[74:75]
	v_pk_add_f32 v[10:11], v[10:11], 1.0 op_sel_hi:[1,0]
	v_pk_add_f32 v[12:13], v[12:13], v[76:77]
	v_pk_add_f32 v[12:13], v[12:13], 1.0 op_sel_hi:[1,0]
	v_pk_add_f32 v[14:15], v[14:15], v[78:79]
	v_pk_add_f32 v[14:15], v[14:15], 1.0 op_sel_hi:[1,0]
	v_pk_add_f32 v[16:17], v[16:17], v[80:81]
	v_pk_add_f32 v[16:17], v[16:17], 1.0 op_sel_hi:[1,0]
	v_pk_add_f32 v[18:19], v[18:19], v[82:83]
	v_pk_add_f32 v[18:19], v[18:19], 1.0 op_sel_hi:[1,0]
	v_pk_add_f32 v[20:21], v[20:21], v[84:85]
	v_pk_add_f32 v[20:21], v[20:21], 1.0 op_sel_hi:[1,0]
	v_pk_add_f32 v[22:23], v[22:23], v[86:87]
	v_pk_add_f32 v[22:23], v[22:23], 1.0 op_sel_hi:[1,0]
	v_pk_add_f32 v[24:25], v[24:25], v[88:89]
	v_pk_add_f32 v[24:25], v[24:25], 1.0 op_sel_hi:[1,0]
	v_pk_add_f32 v[26:27], v[26:27], v[90:91]
	v_pk_add_f32 v[26:27], v[26:27], 1.0 op_sel_hi:[1,0]
	v_pk_add_f32 v[28:29], v[28:29], v[92:93]
	v_pk_add_f32 v[28:29], v[28:29], 1.0 op_sel_hi:[1,0]
	v_pk_add_f32 v[30:31], v[30:31], v[94:95]
	v_pk_add_f32 v[30:31], v[30:31], 1.0 op_sel_hi:[1,0]
	v_pk_add_f32 v[32:33], v[32:33], v[96:97]
	v_pk_add_f32 v[32:33], v[32:33], 1.0 op_sel_hi:[1,0]
	v_pk_add_f32 v[34:35], v[34:35], v[98:99]
	v_pk_add_f32 v[34:35], v[34:35], 1.0 op_sel_hi:[1,0]
	v_pk_add_f32 v[36:37], v[36:37], v[100:101]
	v_pk_add_f32 v[36:37], v[36:37], 1.0 op_sel_hi:[1,0]
	global_load_dwordx4 v[70:73], v160, s[50:51]
	global_load_dwordx4 v[74:77], v160, s[50:51] offset:16
	global_load_dwordx4 v[78:81], v160, s[50:51] offset:2048
	global_load_dwordx4 v[82:85], v160, s[50:51] offset:2064
	global_load_dwordx4 v[86:89], v161, s[50:51]
	global_load_dwordx4 v[90:93], v161, s[50:51] offset:16
	global_load_dwordx4 v[94:97], v161, s[50:51] offset:2048
	global_load_dwordx4 v[98:101], v161, s[50:51] offset:2064
	s_waitcnt vmcnt(0)
	v_pk_mul_f32 v[6:7], v[70:71], v[6:7]
	v_pk_mul_f32 v[8:9], v[72:73], v[8:9]
	v_pk_mul_f32 v[10:11], v[74:75], v[10:11]
	v_pk_mul_f32 v[12:13], v[76:77], v[12:13]
	v_pk_mul_f32 v[14:15], v[78:79], v[14:15]
	v_pk_mul_f32 v[16:17], v[80:81], v[16:17]
	v_pk_mul_f32 v[18:19], v[82:83], v[18:19]
	v_pk_mul_f32 v[20:21], v[84:85], v[20:21]
	v_pk_mul_f32 v[22:23], v[86:87], v[22:23]
	v_pk_mul_f32 v[24:25], v[88:89], v[24:25]
	v_pk_mul_f32 v[26:27], v[90:91], v[26:27]
	v_pk_mul_f32 v[28:29], v[92:93], v[28:29]
	v_pk_mul_f32 v[30:31], v[94:95], v[30:31]
	v_pk_mul_f32 v[32:33], v[96:97], v[32:33]
	v_pk_mul_f32 v[34:35], v[98:99], v[34:35]
	v_pk_mul_f32 v[36:37], v[100:101], v[36:37]
	global_load_dwordx4 v[70:73], v160, s[18:19]
	global_load_dwordx4 v[74:77], v160, s[18:19] offset:16
	global_load_dwordx4 v[78:81], v160, s[18:19] offset:2048
	global_load_dwordx4 v[82:85], v160, s[18:19] offset:2064
	global_load_dwordx4 v[86:89], v161, s[18:19]
	global_load_dwordx4 v[90:93], v161, s[18:19] offset:16
	global_load_dwordx4 v[94:97], v161, s[18:19] offset:2048
	global_load_dwordx4 v[98:101], v161, s[18:19] offset:2064
	s_waitcnt vmcnt(0)
	v_pk_add_f32 v[38:39], v[38:39], v[70:71]
	v_pk_add_f32 v[40:41], v[40:41], v[72:73]
	v_pk_add_f32 v[42:43], v[42:43], v[74:75]
	v_pk_add_f32 v[44:45], v[44:45], v[76:77]
	v_pk_add_f32 v[46:47], v[46:47], v[78:79]
	v_pk_add_f32 v[48:49], v[48:49], v[80:81]
	v_pk_add_f32 v[50:51], v[50:51], v[82:83]
	v_pk_add_f32 v[52:53], v[52:53], v[84:85]
	v_pk_add_f32 v[54:55], v[54:55], v[86:87]
	v_pk_add_f32 v[56:57], v[56:57], v[88:89]
	v_pk_add_f32 v[58:59], v[58:59], v[90:91]
	v_pk_add_f32 v[60:61], v[60:61], v[92:93]
	v_pk_add_f32 v[62:63], v[62:63], v[94:95]
	v_pk_add_f32 v[64:65], v[64:65], v[96:97]
	v_pk_add_f32 v[66:67], v[66:67], v[98:99]
	v_pk_add_f32 v[68:69], v[68:69], v[100:101]
.Lpq_mod_ok_a:
	s_waitcnt vmcnt(4)
	v_lshlrev_b32_e32 v70, 16, v102
	v_and_b32_e32 v71, 0xffff0000, v102
	v_lshlrev_b32_e32 v72, 16, v103
	v_and_b32_e32 v73, 0xffff0000, v103
	v_lshlrev_b32_e32 v74, 16, v104
	v_and_b32_e32 v75, 0xffff0000, v104
	v_lshlrev_b32_e32 v76, 16, v105
	v_and_b32_e32 v77, 0xffff0000, v105
	v_lshlrev_b32_e32 v78, 16, v106
	v_and_b32_e32 v79, 0xffff0000, v106
	v_lshlrev_b32_e32 v80, 16, v107
	v_and_b32_e32 v81, 0xffff0000, v107
	v_lshlrev_b32_e32 v82, 16, v108
	v_and_b32_e32 v83, 0xffff0000, v108
	v_lshlrev_b32_e32 v84, 16, v109
	v_and_b32_e32 v85, 0xffff0000, v109
	v_lshlrev_b32_e32 v86, 16, v110
	v_and_b32_e32 v87, 0xffff0000, v110
	v_lshlrev_b32_e32 v88, 16, v111
	v_and_b32_e32 v89, 0xffff0000, v111
	v_lshlrev_b32_e32 v90, 16, v112
	v_and_b32_e32 v91, 0xffff0000, v112
	v_lshlrev_b32_e32 v92, 16, v113
	v_and_b32_e32 v93, 0xffff0000, v113
	v_lshlrev_b32_e32 v94, 16, v114
	v_and_b32_e32 v95, 0xffff0000, v114
	v_lshlrev_b32_e32 v96, 16, v115
	v_and_b32_e32 v97, 0xffff0000, v115
	v_lshlrev_b32_e32 v98, 16, v116
	v_and_b32_e32 v99, 0xffff0000, v116
	v_lshlrev_b32_e32 v100, 16, v117
	v_and_b32_e32 v101, 0xffff0000, v117
	s_add_u32 s18, s12, 2
	s_sub_u32 s19, s13, 1
	s_min_u32 s18, s18, s19
	s_lshl_b32 s16, s18, 12
	s_add_u32 s52, s38, s16
	s_addc_u32 s53, s39, 0
	global_load_dwordx4 v[102:105], v3, s[52:53]
	global_load_dwordx4 v[106:109], v3, s[52:53] offset:1024
	global_load_dwordx4 v[110:113], v3, s[52:53] offset:2048
	global_load_dwordx4 v[114:117], v3, s[52:53] offset:3072
	v_pk_mul_f32 v[136:137], v[70:71], v[70:71]
	v_pk_fma_f32 v[136:137], v[72:73], v[72:73], v[136:137]
	v_pk_fma_f32 v[136:137], v[74:75], v[74:75], v[136:137]
	v_pk_fma_f32 v[136:137], v[76:77], v[76:77], v[136:137]
	v_pk_fma_f32 v[136:137], v[78:79], v[78:79], v[136:137]
	v_pk_fma_f32 v[136:137], v[80:81], v[80:81], v[136:137]
	v_pk_fma_f32 v[136:137], v[82:83], v[82:83], v[136:137]
	v_pk_fma_f32 v[136:137], v[84:85], v[84:85], v[136:137]
	v_pk_fma_f32 v[136:137], v[86:87], v[86:87], v[136:137]
	v_pk_fma_f32 v[136:137], v[88:89], v[88:89], v[136:137]
	v_pk_fma_f32 v[136:137], v[90:91], v[90:91], v[136:137]
	v_pk_fma_f32 v[136:137], v[92:93], v[92:93], v[136:137]
	v_pk_fma_f32 v[136:137], v[94:95], v[94:95], v[136:137]
	v_pk_fma_f32 v[136:137], v[96:97], v[96:97], v[136:137]
	v_pk_fma_f32 v[136:137], v[98:99], v[98:99], v[136:137]
	v_pk_fma_f32 v[136:137], v[100:101], v[100:101], v[136:137]
	v_add_f32_e32 v136, v136, v137
	s_nop 1
	v_add_f32_dpp v136, v136, v136 quad_perm:[1,0,3,2] row_mask:0xf bank_mask:0xf bound_ctrl:1
	s_nop 1
	v_add_f32_dpp v136, v136, v136 quad_perm:[2,3,0,1] row_mask:0xf bank_mask:0xf bound_ctrl:1
	s_nop 1
	v_add_f32_dpp v136, v136, v136 row_half_mirror row_mask:0xf bank_mask:0xf bound_ctrl:1
	s_nop 1
	v_add_f32_dpp v136, v136, v136 row_mirror row_mask:0xf bank_mask:0xf bound_ctrl:1
	v_mov_b32_e32 v137, v136
	s_nop 1
	v_permlane16_swap_b32_e32 v136, v137
	v_add_f32_e32 v136, v136, v137
	v_mov_b32_e32 v137, v136
	s_nop 1
	v_permlane32_swap_b32_e32 v136, v137
	v_add_f32_e32 v136, v136, v137
	s_mov_b32 s17, 0x800000
	v_fmamk_f32 v136, v136, 0x3a000000, v212
	v_mul_f32_e32 v137, 0x4b800000, v136
	v_cmp_gt_f32_e32 vcc, s17, v136
	s_nop 1
	v_cndmask_b32_e32 v136, v136, v137, vcc
	v_rsq_f32_e32 v136, v136
	s_nop 0
	v_mul_f32_e32 v137, 0x45800000, v136
	v_cndmask_b32_e32 v136, v136, v137, vcc
	v_mov_b32_e32 v137, v136
	v_pk_mul_f32 v[70:71], v[70:71], v[136:137]
	v_pk_mul_f32 v[72:73], v[72:73], v[136:137]
	v_pk_mul_f32 v[74:75], v[74:75], v[136:137]
	v_pk_mul_f32 v[76:77], v[76:77], v[136:137]
	v_pk_mul_f32 v[78:79], v[78:79], v[136:137]
	v_pk_mul_f32 v[80:81], v[80:81], v[136:137]
	v_pk_mul_f32 v[82:83], v[82:83], v[136:137]
	v_pk_mul_f32 v[84:85], v[84:85], v[136:137]
	v_pk_mul_f32 v[86:87], v[86:87], v[136:137]
	v_pk_mul_f32 v[88:89], v[88:89], v[136:137]
	v_pk_mul_f32 v[90:91], v[90:91], v[136:137]
	v_pk_mul_f32 v[92:93], v[92:93], v[136:137]
	v_pk_mul_f32 v[94:95], v[94:95], v[136:137]
	v_pk_mul_f32 v[96:97], v[96:97], v[136:137]
	v_pk_mul_f32 v[98:99], v[98:99], v[136:137]
	v_pk_mul_f32 v[100:101], v[100:101], v[136:137]
	v_pk_fma_f32 v[70:71], v[70:71], v[6:7], v[38:39]
	v_pk_fma_f32 v[72:73], v[72:73], v[8:9], v[40:41]
	v_pk_fma_f32 v[74:75], v[74:75], v[10:11], v[42:43]
	v_pk_fma_f32 v[76:77], v[76:77], v[12:13], v[44:45]
	v_pk_fma_f32 v[78:79], v[78:79], v[14:15], v[46:47]
	v_pk_fma_f32 v[80:81], v[80:81], v[16:17], v[48:49]
	v_pk_fma_f32 v[82:83], v[82:83], v[18:19], v[50:51]
	v_pk_fma_f32 v[84:85], v[84:85], v[20:21], v[52:53]
	v_pk_fma_f32 v[86:87], v[86:87], v[22:23], v[54:55]
	v_pk_fma_f32 v[88:89], v[88:89], v[24:25], v[56:57]
	v_pk_fma_f32 v[90:91], v[90:91], v[26:27], v[58:59]
	v_pk_fma_f32 v[92:93], v[92:93], v[28:29], v[60:61]
	v_pk_fma_f32 v[94:95], v[94:95], v[30:31], v[62:63]
	v_pk_fma_f32 v[96:97], v[96:97], v[32:33], v[64:65]
	v_pk_fma_f32 v[98:99], v[98:99], v[34:35], v[66:67]
	v_pk_fma_f32 v[100:101], v[100:101], v[36:37], v[68:69]
	v_cvt_pk_bf16_f32 v70, v70, v71
	v_cvt_pk_bf16_f32 v71, v72, v73
	v_cvt_pk_bf16_f32 v72, v74, v75
	v_cvt_pk_bf16_f32 v73, v76, v77
	v_cvt_pk_bf16_f32 v78, v78, v79
	v_cvt_pk_bf16_f32 v79, v80, v81
	v_cvt_pk_bf16_f32 v80, v82, v83
	v_cvt_pk_bf16_f32 v81, v84, v85
	v_cvt_pk_bf16_f32 v86, v86, v87
	v_cvt_pk_bf16_f32 v87, v88, v89
	v_cvt_pk_bf16_f32 v88, v90, v91
	v_cvt_pk_bf16_f32 v89, v92, v93
	v_cvt_pk_bf16_f32 v94, v94, v95
	v_cvt_pk_bf16_f32 v95, v96, v97
	v_cvt_pk_bf16_f32 v96, v98, v99
	v_cvt_pk_bf16_f32 v97, v100, v101
	s_lshl_b32 s16, s12, 12
	s_add_u32 s52, s42, s16
	s_addc_u32 s53, s43, 0
	global_store_dwordx4 v3, v[70:73], s[52:53]
	global_store_dwordx4 v3, v[78:81], s[52:53] offset:1024
	global_store_dwordx4 v3, v[86:89], s[52:53] offset:2048
	global_store_dwordx4 v3, v[94:97], s[52:53] offset:3072
	s_add_u32 s12, s12, 1
	s_cmp_ge_u32 s12, s13
	s_cbranch_scc1 .Lpq_end
.Lpq_loop:
	s_lshr_b32 s16, s12, 12
	s_cmp_lt_u32 s12, 0x4000
	s_cselect_b32 s16, s16, 4
	s_cmp_eq_u32 s16, s15
	s_cbranch_scc1 .Lpq_mod_ok_b
	s_mov_b32 s15, s16
	s_mul_i32 s16, s16, 0xc000
	s_add_u32 s52, s46, s16
	s_addc_u32 s53, s47, 0
	s_add_u32 s10, s52, 0x8000
	s_addc_u32 s11, s53, 0
	s_add_u32 s52, s52, 0x6000
	s_addc_u32 s53, s53, 0
	s_add_u32 s16, s48, 0x8000
	s_addc_u32 s17, s49, 0
	s_add_u32 s18, s48, 0x6000
	s_addc_u32 s19, s49, 0
	global_load_dwordx4 v[6:9], v160, s[10:11]
	global_load_dwordx4 v[70:73], v160, s[16:17]
	global_load_dwordx4 v[38:41], v160, s[52:53]
	global_load_dwordx4 v[10:13], v160, s[10:11] offset:16
	global_load_dwordx4 v[74:77], v160, s[16:17] offset:16
	global_load_dwordx4 v[42:45], v160, s[52:53] offset:16
	global_load_dwordx4 v[14:17], v160, s[10:11] offset:2048
	global_load_dwordx4 v[78:81], v160, s[16:17] offset:2048
	global_load_dwordx4 v[46:49], v160, s[52:53] offset:2048
	global_load_dwordx4 v[18:21], v160, s[10:11] offset:2064
	global_load_dwordx4 v[82:85], v160, s[16:17] offset:2064
	global_load_dwordx4 v[50:53], v160, s[52:53] offset:2064
	global_load_dwordx4 v[22:25], v161, s[10:11]
	global_load_dwordx4 v[86:89], v161, s[16:17]
	global_load_dwordx4 v[54:57], v161, s[52:53]
	global_load_dwordx4 v[26:29], v161, s[10:11] offset:16
	global_load_dwordx4 v[90:93], v161, s[16:17] offset:16
	global_load_dwordx4 v[58:61], v161, s[52:53] offset:16
	global_load_dwordx4 v[30:33], v161, s[10:11] offset:2048
	global_load_dwordx4 v[94:97], v161, s[16:17] offset:2048
	global_load_dwordx4 v[62:65], v161, s[52:53] offset:2048
	global_load_dwordx4 v[34:37], v161, s[10:11] offset:2064
	global_load_dwordx4 v[98:101], v161, s[16:17] offset:2064
	global_load_dwordx4 v[66:69], v161, s[52:53] offset:2064
	s_waitcnt vmcnt(0)
	v_pk_add_f32 v[6:7], v[6:7], v[70:71]
	v_pk_add_f32 v[6:7], v[6:7], 1.0 op_sel_hi:[1,0]
	v_pk_add_f32 v[8:9], v[8:9], v[72:73]
	v_pk_add_f32 v[8:9], v[8:9], 1.0 op_sel_hi:[1,0]
	v_pk_add_f32 v[10:11], v[10:11], v[74:75]
	v_pk_add_f32 v[10:11], v[10:11], 1.0 op_sel_hi:[1,0]
	v_pk_add_f32 v[12:13], v[12:13], v[76:77]
	v_pk_add_f32 v[12:13], v[12:13], 1.0 op_sel_hi:[1,0]
	v_pk_add_f32 v[14:15], v[14:15], v[78:79]
	v_pk_add_f32 v[14:15], v[14:15], 1.0 op_sel_hi:[1,0]
	v_pk_add_f32 v[16:17], v[16:17], v[80:81]
	v_pk_add_f32 v[16:17], v[16:17], 1.0 op_sel_hi:[1,0]
	v_pk_add_f32 v[18:19], v[18:19], v[82:83]
	v_pk_add_f32 v[18:19], v[18:19], 1.0 op_sel_hi:[1,0]
	v_pk_add_f32 v[20:21], v[20:21], v[84:85]
	v_pk_add_f32 v[20:21], v[20:21], 1.0 op_sel_hi:[1,0]
	v_pk_add_f32 v[22:23], v[22:23], v[86:87]
	v_pk_add_f32 v[22:23], v[22:23], 1.0 op_sel_hi:[1,0]
	v_pk_add_f32 v[24:25], v[24:25], v[88:89]
	v_pk_add_f32 v[24:25], v[24:25], 1.0 op_sel_hi:[1,0]
	v_pk_add_f32 v[26:27], v[26:27], v[90:91]
	v_pk_add_f32 v[26:27], v[26:27], 1.0 op_sel_hi:[1,0]
	v_pk_add_f32 v[28:29], v[28:29], v[92:93]
	v_pk_add_f32 v[28:29], v[28:29], 1.0 op_sel_hi:[1,0]
	v_pk_add_f32 v[30:31], v[30:31], v[94:95]
	v_pk_add_f32 v[30:31], v[30:31], 1.0 op_sel_hi:[1,0]
	v_pk_add_f32 v[32:33], v[32:33], v[96:97]
	v_pk_add_f32 v[32:33], v[32:33], 1.0 op_sel_hi:[1,0]
	v_pk_add_f32 v[34:35], v[34:35], v[98:99]
	v_pk_add_f32 v[34:35], v[34:35], 1.0 op_sel_hi:[1,0]
	v_pk_add_f32 v[36:37], v[36:37], v[100:101]
	v_pk_add_f32 v[36:37], v[36:37], 1.0 op_sel_hi:[1,0]
	global_load_dwordx4 v[70:73], v160, s[50:51]
	global_load_dwordx4 v[74:77], v160, s[50:51] offset:16
	global_load_dwordx4 v[78:81], v160, s[50:51] offset:2048
	global_load_dwordx4 v[82:85], v160, s[50:51] offset:2064
	global_load_dwordx4 v[86:89], v161, s[50:51]
	global_load_dwordx4 v[90:93], v161, s[50:51] offset:16
	global_load_dwordx4 v[94:97], v161, s[50:51] offset:2048
	global_load_dwordx4 v[98:101], v161, s[50:51] offset:2064
	s_waitcnt vmcnt(0)
	v_pk_mul_f32 v[6:7], v[70:71], v[6:7]
	v_pk_mul_f32 v[8:9], v[72:73], v[8:9]
	v_pk_mul_f32 v[10:11], v[74:75], v[10:11]
	v_pk_mul_f32 v[12:13], v[76:77], v[12:13]
	v_pk_mul_f32 v[14:15], v[78:79], v[14:15]
	v_pk_mul_f32 v[16:17], v[80:81], v[16:17]
	v_pk_mul_f32 v[18:19], v[82:83], v[18:19]
	v_pk_mul_f32 v[20:21], v[84:85], v[20:21]
	v_pk_mul_f32 v[22:23], v[86:87], v[22:23]
	v_pk_mul_f32 v[24:25], v[88:89], v[24:25]
	v_pk_mul_f32 v[26:27], v[90:91], v[26:27]
	v_pk_mul_f32 v[28:29], v[92:93], v[28:29]
	v_pk_mul_f32 v[30:31], v[94:95], v[30:31]
	v_pk_mul_f32 v[32:33], v[96:97], v[32:33]
	v_pk_mul_f32 v[34:35], v[98:99], v[34:35]
	v_pk_mul_f32 v[36:37], v[100:101], v[36:37]
	global_load_dwordx4 v[70:73], v160, s[18:19]
	global_load_dwordx4 v[74:77], v160, s[18:19] offset:16
	global_load_dwordx4 v[78:81], v160, s[18:19] offset:2048
	global_load_dwordx4 v[82:85], v160, s[18:19] offset:2064
	global_load_dwordx4 v[86:89], v161, s[18:19]
	global_load_dwordx4 v[90:93], v161, s[18:19] offset:16
	global_load_dwordx4 v[94:97], v161, s[18:19] offset:2048
	global_load_dwordx4 v[98:101], v161, s[18:19] offset:2064
	s_waitcnt vmcnt(0)
	v_pk_add_f32 v[38:39], v[38:39], v[70:71]
	v_pk_add_f32 v[40:41], v[40:41], v[72:73]
	v_pk_add_f32 v[42:43], v[42:43], v[74:75]
	v_pk_add_f32 v[44:45], v[44:45], v[76:77]
	v_pk_add_f32 v[46:47], v[46:47], v[78:79]
	v_pk_add_f32 v[48:49], v[48:49], v[80:81]
	v_pk_add_f32 v[50:51], v[50:51], v[82:83]
	v_pk_add_f32 v[52:53], v[52:53], v[84:85]
	v_pk_add_f32 v[54:55], v[54:55], v[86:87]
	v_pk_add_f32 v[56:57], v[56:57], v[88:89]
	v_pk_add_f32 v[58:59], v[58:59], v[90:91]
	v_pk_add_f32 v[60:61], v[60:61], v[92:93]
	v_pk_add_f32 v[62:63], v[62:63], v[94:95]
	v_pk_add_f32 v[64:65], v[64:65], v[96:97]
	v_pk_add_f32 v[66:67], v[66:67], v[98:99]
	v_pk_add_f32 v[68:69], v[68:69], v[100:101]
.Lpq_mod_ok_b:
	s_waitcnt vmcnt(8)
	v_lshlrev_b32_e32 v70, 16, v118
	v_and_b32_e32 v71, 0xffff0000, v118
	v_lshlrev_b32_e32 v72, 16, v119
	v_and_b32_e32 v73, 0xffff0000, v119
	v_lshlrev_b32_e32 v74, 16, v120
	v_and_b32_e32 v75, 0xffff0000, v120
	v_lshlrev_b32_e32 v76, 16, v121
	v_and_b32_e32 v77, 0xffff0000, v121
	v_lshlrev_b32_e32 v78, 16, v122
	v_and_b32_e32 v79, 0xffff0000, v122
	v_lshlrev_b32_e32 v80, 16, v123
	v_and_b32_e32 v81, 0xffff0000, v123
	v_lshlrev_b32_e32 v82, 16, v124
	v_and_b32_e32 v83, 0xffff0000, v124
	v_lshlrev_b32_e32 v84, 16, v125
	v_and_b32_e32 v85, 0xffff0000, v125
	v_lshlrev_b32_e32 v86, 16, v126
	v_and_b32_e32 v87, 0xffff0000, v126
	v_lshlrev_b32_e32 v88, 16, v127
	v_and_b32_e32 v89, 0xffff0000, v127
	v_lshlrev_b32_e32 v90, 16, v128
	v_and_b32_e32 v91, 0xffff0000, v128
	v_lshlrev_b32_e32 v92, 16, v129
	v_and_b32_e32 v93, 0xffff0000, v129
	v_lshlrev_b32_e32 v94, 16, v130
	v_and_b32_e32 v95, 0xffff0000, v130
	v_lshlrev_b32_e32 v96, 16, v131
	v_and_b32_e32 v97, 0xffff0000, v131
	v_lshlrev_b32_e32 v98, 16, v132
	v_and_b32_e32 v99, 0xffff0000, v132
	v_lshlrev_b32_e32 v100, 16, v133
	v_and_b32_e32 v101, 0xffff0000, v133
	s_add_u32 s18, s12, 2
	s_sub_u32 s19, s13, 1
	s_min_u32 s18, s18, s19
	s_lshl_b32 s16, s18, 12
	s_add_u32 s52, s38, s16
	s_addc_u32 s53, s39, 0
	global_load_dwordx4 v[118:121], v3, s[52:53]
	global_load_dwordx4 v[122:125], v3, s[52:53] offset:1024
	global_load_dwordx4 v[126:129], v3, s[52:53] offset:2048
	global_load_dwordx4 v[130:133], v3, s[52:53] offset:3072
	v_pk_mul_f32 v[136:137], v[70:71], v[70:71]
	v_pk_fma_f32 v[136:137], v[72:73], v[72:73], v[136:137]
	v_pk_fma_f32 v[136:137], v[74:75], v[74:75], v[136:137]
	v_pk_fma_f32 v[136:137], v[76:77], v[76:77], v[136:137]
	v_pk_fma_f32 v[136:137], v[78:79], v[78:79], v[136:137]
	v_pk_fma_f32 v[136:137], v[80:81], v[80:81], v[136:137]
	v_pk_fma_f32 v[136:137], v[82:83], v[82:83], v[136:137]
	v_pk_fma_f32 v[136:137], v[84:85], v[84:85], v[136:137]
	v_pk_fma_f32 v[136:137], v[86:87], v[86:87], v[136:137]
	v_pk_fma_f32 v[136:137], v[88:89], v[88:89], v[136:137]
	v_pk_fma_f32 v[136:137], v[90:91], v[90:91], v[136:137]
	v_pk_fma_f32 v[136:137], v[92:93], v[92:93], v[136:137]
	v_pk_fma_f32 v[136:137], v[94:95], v[94:95], v[136:137]
	v_pk_fma_f32 v[136:137], v[96:97], v[96:97], v[136:137]
	v_pk_fma_f32 v[136:137], v[98:99], v[98:99], v[136:137]
	v_pk_fma_f32 v[136:137], v[100:101], v[100:101], v[136:137]
	v_add_f32_e32 v136, v136, v137
	s_nop 1
	v_add_f32_dpp v136, v136, v136 quad_perm:[1,0,3,2] row_mask:0xf bank_mask:0xf bound_ctrl:1
	s_nop 1
	v_add_f32_dpp v136, v136, v136 quad_perm:[2,3,0,1] row_mask:0xf bank_mask:0xf bound_ctrl:1
	s_nop 1
	v_add_f32_dpp v136, v136, v136 row_half_mirror row_mask:0xf bank_mask:0xf bound_ctrl:1
	s_nop 1
	v_add_f32_dpp v136, v136, v136 row_mirror row_mask:0xf bank_mask:0xf bound_ctrl:1
	v_mov_b32_e32 v137, v136
	s_nop 1
	v_permlane16_swap_b32_e32 v136, v137
	v_add_f32_e32 v136, v136, v137
	v_mov_b32_e32 v137, v136
	s_nop 1
	v_permlane32_swap_b32_e32 v136, v137
	v_add_f32_e32 v136, v136, v137
	s_mov_b32 s17, 0x800000
	v_fmamk_f32 v136, v136, 0x3a000000, v212
	v_mul_f32_e32 v137, 0x4b800000, v136
	v_cmp_gt_f32_e32 vcc, s17, v136
	s_nop 1
	v_cndmask_b32_e32 v136, v136, v137, vcc
	v_rsq_f32_e32 v136, v136
	s_nop 0
	v_mul_f32_e32 v137, 0x45800000, v136
	v_cndmask_b32_e32 v136, v136, v137, vcc
	v_mov_b32_e32 v137, v136
	v_pk_mul_f32 v[70:71], v[70:71], v[136:137]
	v_pk_mul_f32 v[72:73], v[72:73], v[136:137]
	v_pk_mul_f32 v[74:75], v[74:75], v[136:137]
	v_pk_mul_f32 v[76:77], v[76:77], v[136:137]
	v_pk_mul_f32 v[78:79], v[78:79], v[136:137]
	v_pk_mul_f32 v[80:81], v[80:81], v[136:137]
	v_pk_mul_f32 v[82:83], v[82:83], v[136:137]
	v_pk_mul_f32 v[84:85], v[84:85], v[136:137]
	v_pk_mul_f32 v[86:87], v[86:87], v[136:137]
	v_pk_mul_f32 v[88:89], v[88:89], v[136:137]
	v_pk_mul_f32 v[90:91], v[90:91], v[136:137]
	v_pk_mul_f32 v[92:93], v[92:93], v[136:137]
	v_pk_mul_f32 v[94:95], v[94:95], v[136:137]
	v_pk_mul_f32 v[96:97], v[96:97], v[136:137]
	v_pk_mul_f32 v[98:99], v[98:99], v[136:137]
	v_pk_mul_f32 v[100:101], v[100:101], v[136:137]
	v_pk_fma_f32 v[70:71], v[70:71], v[6:7], v[38:39]
	v_pk_fma_f32 v[72:73], v[72:73], v[8:9], v[40:41]
	v_pk_fma_f32 v[74:75], v[74:75], v[10:11], v[42:43]
	v_pk_fma_f32 v[76:77], v[76:77], v[12:13], v[44:45]
	v_pk_fma_f32 v[78:79], v[78:79], v[14:15], v[46:47]
	v_pk_fma_f32 v[80:81], v[80:81], v[16:17], v[48:49]
	v_pk_fma_f32 v[82:83], v[82:83], v[18:19], v[50:51]
	v_pk_fma_f32 v[84:85], v[84:85], v[20:21], v[52:53]
	v_pk_fma_f32 v[86:87], v[86:87], v[22:23], v[54:55]
	v_pk_fma_f32 v[88:89], v[88:89], v[24:25], v[56:57]
	v_pk_fma_f32 v[90:91], v[90:91], v[26:27], v[58:59]
	v_pk_fma_f32 v[92:93], v[92:93], v[28:29], v[60:61]
	v_pk_fma_f32 v[94:95], v[94:95], v[30:31], v[62:63]
	v_pk_fma_f32 v[96:97], v[96:97], v[32:33], v[64:65]
	v_pk_fma_f32 v[98:99], v[98:99], v[34:35], v[66:67]
	v_pk_fma_f32 v[100:101], v[100:101], v[36:37], v[68:69]
	v_cvt_pk_bf16_f32 v70, v70, v71
	v_cvt_pk_bf16_f32 v71, v72, v73
	v_cvt_pk_bf16_f32 v72, v74, v75
	v_cvt_pk_bf16_f32 v73, v76, v77
	v_cvt_pk_bf16_f32 v78, v78, v79
	v_cvt_pk_bf16_f32 v79, v80, v81
	v_cvt_pk_bf16_f32 v80, v82, v83
	v_cvt_pk_bf16_f32 v81, v84, v85
	v_cvt_pk_bf16_f32 v86, v86, v87
	v_cvt_pk_bf16_f32 v87, v88, v89
	v_cvt_pk_bf16_f32 v88, v90, v91
	v_cvt_pk_bf16_f32 v89, v92, v93
	v_cvt_pk_bf16_f32 v94, v94, v95
	v_cvt_pk_bf16_f32 v95, v96, v97
	v_cvt_pk_bf16_f32 v96, v98, v99
	v_cvt_pk_bf16_f32 v97, v100, v101
	s_lshl_b32 s16, s12, 12
	s_add_u32 s52, s42, s16
	s_addc_u32 s53, s43, 0
	global_store_dwordx4 v3, v[70:73], s[52:53]
	global_store_dwordx4 v3, v[78:81], s[52:53] offset:1024
	global_store_dwordx4 v3, v[86:89], s[52:53] offset:2048
	global_store_dwordx4 v3, v[94:97], s[52:53] offset:3072
	s_add_u32 s12, s12, 1
	s_cmp_ge_u32 s12, s13
	s_cbranch_scc1 .Lpq_end
	s_lshr_b32 s16, s12, 12
	s_cmp_lt_u32 s12, 0x4000
	s_cselect_b32 s16, s16, 4
	s_cmp_eq_u32 s16, s15
	s_cbranch_scc1 .Lpq_mod_ok_c
	s_mov_b32 s15, s16
	s_mul_i32 s16, s16, 0xc000
	s_add_u32 s52, s46, s16
	s_addc_u32 s53, s47, 0
	s_add_u32 s10, s52, 0x8000
	s_addc_u32 s11, s53, 0
	s_add_u32 s52, s52, 0x6000
	s_addc_u32 s53, s53, 0
	s_add_u32 s16, s48, 0x8000
	s_addc_u32 s17, s49, 0
	s_add_u32 s18, s48, 0x6000
	s_addc_u32 s19, s49, 0
	global_load_dwordx4 v[6:9], v160, s[10:11]
	global_load_dwordx4 v[70:73], v160, s[16:17]
	global_load_dwordx4 v[38:41], v160, s[52:53]
	global_load_dwordx4 v[10:13], v160, s[10:11] offset:16
	global_load_dwordx4 v[74:77], v160, s[16:17] offset:16
	global_load_dwordx4 v[42:45], v160, s[52:53] offset:16
	global_load_dwordx4 v[14:17], v160, s[10:11] offset:2048
	global_load_dwordx4 v[78:81], v160, s[16:17] offset:2048
	global_load_dwordx4 v[46:49], v160, s[52:53] offset:2048
	global_load_dwordx4 v[18:21], v160, s[10:11] offset:2064
	global_load_dwordx4 v[82:85], v160, s[16:17] offset:2064
	global_load_dwordx4 v[50:53], v160, s[52:53] offset:2064
	global_load_dwordx4 v[22:25], v161, s[10:11]
	global_load_dwordx4 v[86:89], v161, s[16:17]
	global_load_dwordx4 v[54:57], v161, s[52:53]
	global_load_dwordx4 v[26:29], v161, s[10:11] offset:16
	global_load_dwordx4 v[90:93], v161, s[16:17] offset:16
	global_load_dwordx4 v[58:61], v161, s[52:53] offset:16
	global_load_dwordx4 v[30:33], v161, s[10:11] offset:2048
	global_load_dwordx4 v[94:97], v161, s[16:17] offset:2048
	global_load_dwordx4 v[62:65], v161, s[52:53] offset:2048
	global_load_dwordx4 v[34:37], v161, s[10:11] offset:2064
	global_load_dwordx4 v[98:101], v161, s[16:17] offset:2064
	global_load_dwordx4 v[66:69], v161, s[52:53] offset:2064
	s_waitcnt vmcnt(0)
	v_pk_add_f32 v[6:7], v[6:7], v[70:71]
	v_pk_add_f32 v[6:7], v[6:7], 1.0 op_sel_hi:[1,0]
	v_pk_add_f32 v[8:9], v[8:9], v[72:73]
	v_pk_add_f32 v[8:9], v[8:9], 1.0 op_sel_hi:[1,0]
	v_pk_add_f32 v[10:11], v[10:11], v[74:75]
	v_pk_add_f32 v[10:11], v[10:11], 1.0 op_sel_hi:[1,0]
	v_pk_add_f32 v[12:13], v[12:13], v[76:77]
	v_pk_add_f32 v[12:13], v[12:13], 1.0 op_sel_hi:[1,0]
	v_pk_add_f32 v[14:15], v[14:15], v[78:79]
	v_pk_add_f32 v[14:15], v[14:15], 1.0 op_sel_hi:[1,0]
	v_pk_add_f32 v[16:17], v[16:17], v[80:81]
	v_pk_add_f32 v[16:17], v[16:17], 1.0 op_sel_hi:[1,0]
	v_pk_add_f32 v[18:19], v[18:19], v[82:83]
	v_pk_add_f32 v[18:19], v[18:19], 1.0 op_sel_hi:[1,0]
	v_pk_add_f32 v[20:21], v[20:21], v[84:85]
	v_pk_add_f32 v[20:21], v[20:21], 1.0 op_sel_hi:[1,0]
	v_pk_add_f32 v[22:23], v[22:23], v[86:87]
	v_pk_add_f32 v[22:23], v[22:23], 1.0 op_sel_hi:[1,0]
	v_pk_add_f32 v[24:25], v[24:25], v[88:89]
	v_pk_add_f32 v[24:25], v[24:25], 1.0 op_sel_hi:[1,0]
	v_pk_add_f32 v[26:27], v[26:27], v[90:91]
	v_pk_add_f32 v[26:27], v[26:27], 1.0 op_sel_hi:[1,0]
	v_pk_add_f32 v[28:29], v[28:29], v[92:93]
	v_pk_add_f32 v[28:29], v[28:29], 1.0 op_sel_hi:[1,0]
	v_pk_add_f32 v[30:31], v[30:31], v[94:95]
	v_pk_add_f32 v[30:31], v[30:31], 1.0 op_sel_hi:[1,0]
	v_pk_add_f32 v[32:33], v[32:33], v[96:97]
	v_pk_add_f32 v[32:33], v[32:33], 1.0 op_sel_hi:[1,0]
	v_pk_add_f32 v[34:35], v[34:35], v[98:99]
	v_pk_add_f32 v[34:35], v[34:35], 1.0 op_sel_hi:[1,0]
	v_pk_add_f32 v[36:37], v[36:37], v[100:101]
	v_pk_add_f32 v[36:37], v[36:37], 1.0 op_sel_hi:[1,0]
	global_load_dwordx4 v[70:73], v160, s[50:51]
	global_load_dwordx4 v[74:77], v160, s[50:51] offset:16
	global_load_dwordx4 v[78:81], v160, s[50:51] offset:2048
	global_load_dwordx4 v[82:85], v160, s[50:51] offset:2064
	global_load_dwordx4 v[86:89], v161, s[50:51]
	global_load_dwordx4 v[90:93], v161, s[50:51] offset:16
	global_load_dwordx4 v[94:97], v161, s[50:51] offset:2048
	global_load_dwordx4 v[98:101], v161, s[50:51] offset:2064
	s_waitcnt vmcnt(0)
	v_pk_mul_f32 v[6:7], v[70:71], v[6:7]
	v_pk_mul_f32 v[8:9], v[72:73], v[8:9]
	v_pk_mul_f32 v[10:11], v[74:75], v[10:11]
	v_pk_mul_f32 v[12:13], v[76:77], v[12:13]
	v_pk_mul_f32 v[14:15], v[78:79], v[14:15]
	v_pk_mul_f32 v[16:17], v[80:81], v[16:17]
	v_pk_mul_f32 v[18:19], v[82:83], v[18:19]
	v_pk_mul_f32 v[20:21], v[84:85], v[20:21]
	v_pk_mul_f32 v[22:23], v[86:87], v[22:23]
	v_pk_mul_f32 v[24:25], v[88:89], v[24:25]
	v_pk_mul_f32 v[26:27], v[90:91], v[26:27]
	v_pk_mul_f32 v[28:29], v[92:93], v[28:29]
	v_pk_mul_f32 v[30:31], v[94:95], v[30:31]
	v_pk_mul_f32 v[32:33], v[96:97], v[32:33]
	v_pk_mul_f32 v[34:35], v[98:99], v[34:35]
	v_pk_mul_f32 v[36:37], v[100:101], v[36:37]
	global_load_dwordx4 v[70:73], v160, s[18:19]
	global_load_dwordx4 v[74:77], v160, s[18:19] offset:16
	global_load_dwordx4 v[78:81], v160, s[18:19] offset:2048
	global_load_dwordx4 v[82:85], v160, s[18:19] offset:2064
	global_load_dwordx4 v[86:89], v161, s[18:19]
	global_load_dwordx4 v[90:93], v161, s[18:19] offset:16
	global_load_dwordx4 v[94:97], v161, s[18:19] offset:2048
	global_load_dwordx4 v[98:101], v161, s[18:19] offset:2064
	s_waitcnt vmcnt(0)
	v_pk_add_f32 v[38:39], v[38:39], v[70:71]
	v_pk_add_f32 v[40:41], v[40:41], v[72:73]
	v_pk_add_f32 v[42:43], v[42:43], v[74:75]
	v_pk_add_f32 v[44:45], v[44:45], v[76:77]
	v_pk_add_f32 v[46:47], v[46:47], v[78:79]
	v_pk_add_f32 v[48:49], v[48:49], v[80:81]
	v_pk_add_f32 v[50:51], v[50:51], v[82:83]
	v_pk_add_f32 v[52:53], v[52:53], v[84:85]
	v_pk_add_f32 v[54:55], v[54:55], v[86:87]
	v_pk_add_f32 v[56:57], v[56:57], v[88:89]
	v_pk_add_f32 v[58:59], v[58:59], v[90:91]
	v_pk_add_f32 v[60:61], v[60:61], v[92:93]
	v_pk_add_f32 v[62:63], v[62:63], v[94:95]
	v_pk_add_f32 v[64:65], v[64:65], v[96:97]
	v_pk_add_f32 v[66:67], v[66:67], v[98:99]
	v_pk_add_f32 v[68:69], v[68:69], v[100:101]
.Lpq_mod_ok_c:
	s_waitcnt vmcnt(8)
	v_lshlrev_b32_e32 v70, 16, v102
	v_and_b32_e32 v71, 0xffff0000, v102
	v_lshlrev_b32_e32 v72, 16, v103
	v_and_b32_e32 v73, 0xffff0000, v103
	v_lshlrev_b32_e32 v74, 16, v104
	v_and_b32_e32 v75, 0xffff0000, v104
	v_lshlrev_b32_e32 v76, 16, v105
	v_and_b32_e32 v77, 0xffff0000, v105
	v_lshlrev_b32_e32 v78, 16, v106
	v_and_b32_e32 v79, 0xffff0000, v106
	v_lshlrev_b32_e32 v80, 16, v107
	v_and_b32_e32 v81, 0xffff0000, v107
	v_lshlrev_b32_e32 v82, 16, v108
	v_and_b32_e32 v83, 0xffff0000, v108
	v_lshlrev_b32_e32 v84, 16, v109
	v_and_b32_e32 v85, 0xffff0000, v109
	v_lshlrev_b32_e32 v86, 16, v110
	v_and_b32_e32 v87, 0xffff0000, v110
	v_lshlrev_b32_e32 v88, 16, v111
	v_and_b32_e32 v89, 0xffff0000, v111
	v_lshlrev_b32_e32 v90, 16, v112
	v_and_b32_e32 v91, 0xffff0000, v112
	v_lshlrev_b32_e32 v92, 16, v113
	v_and_b32_e32 v93, 0xffff0000, v113
	v_lshlrev_b32_e32 v94, 16, v114
	v_and_b32_e32 v95, 0xffff0000, v114
	v_lshlrev_b32_e32 v96, 16, v115
	v_and_b32_e32 v97, 0xffff0000, v115
	v_lshlrev_b32_e32 v98, 16, v116
	v_and_b32_e32 v99, 0xffff0000, v116
	v_lshlrev_b32_e32 v100, 16, v117
	v_and_b32_e32 v101, 0xffff0000, v117
	s_add_u32 s18, s12, 2
	s_sub_u32 s19, s13, 1
	s_min_u32 s18, s18, s19
	s_lshl_b32 s16, s18, 12
	s_add_u32 s52, s38, s16
	s_addc_u32 s53, s39, 0
	global_load_dwordx4 v[102:105], v3, s[52:53]
	global_load_dwordx4 v[106:109], v3, s[52:53] offset:1024
	global_load_dwordx4 v[110:113], v3, s[52:53] offset:2048
	global_load_dwordx4 v[114:117], v3, s[52:53] offset:3072
	v_pk_mul_f32 v[136:137], v[70:71], v[70:71]
	v_pk_fma_f32 v[136:137], v[72:73], v[72:73], v[136:137]
	v_pk_fma_f32 v[136:137], v[74:75], v[74:75], v[136:137]
	v_pk_fma_f32 v[136:137], v[76:77], v[76:77], v[136:137]
	v_pk_fma_f32 v[136:137], v[78:79], v[78:79], v[136:137]
	v_pk_fma_f32 v[136:137], v[80:81], v[80:81], v[136:137]
	v_pk_fma_f32 v[136:137], v[82:83], v[82:83], v[136:137]
	v_pk_fma_f32 v[136:137], v[84:85], v[84:85], v[136:137]
	v_pk_fma_f32 v[136:137], v[86:87], v[86:87], v[136:137]
	v_pk_fma_f32 v[136:137], v[88:89], v[88:89], v[136:137]
	v_pk_fma_f32 v[136:137], v[90:91], v[90:91], v[136:137]
	v_pk_fma_f32 v[136:137], v[92:93], v[92:93], v[136:137]
	v_pk_fma_f32 v[136:137], v[94:95], v[94:95], v[136:137]
	v_pk_fma_f32 v[136:137], v[96:97], v[96:97], v[136:137]
	v_pk_fma_f32 v[136:137], v[98:99], v[98:99], v[136:137]
	v_pk_fma_f32 v[136:137], v[100:101], v[100:101], v[136:137]
	v_add_f32_e32 v136, v136, v137
	s_nop 1
	v_add_f32_dpp v136, v136, v136 quad_perm:[1,0,3,2] row_mask:0xf bank_mask:0xf bound_ctrl:1
	s_nop 1
	v_add_f32_dpp v136, v136, v136 quad_perm:[2,3,0,1] row_mask:0xf bank_mask:0xf bound_ctrl:1
	s_nop 1
	v_add_f32_dpp v136, v136, v136 row_half_mirror row_mask:0xf bank_mask:0xf bound_ctrl:1
	s_nop 1
	v_add_f32_dpp v136, v136, v136 row_mirror row_mask:0xf bank_mask:0xf bound_ctrl:1
	v_mov_b32_e32 v137, v136
	s_nop 1
	v_permlane16_swap_b32_e32 v136, v137
	v_add_f32_e32 v136, v136, v137
	v_mov_b32_e32 v137, v136
	s_nop 1
	v_permlane32_swap_b32_e32 v136, v137
	v_add_f32_e32 v136, v136, v137
	s_mov_b32 s17, 0x800000
	v_fmamk_f32 v136, v136, 0x3a000000, v212
	v_mul_f32_e32 v137, 0x4b800000, v136
	v_cmp_gt_f32_e32 vcc, s17, v136
	s_nop 1
	v_cndmask_b32_e32 v136, v136, v137, vcc
	v_rsq_f32_e32 v136, v136
	s_nop 0
	v_mul_f32_e32 v137, 0x45800000, v136
	v_cndmask_b32_e32 v136, v136, v137, vcc
	v_mov_b32_e32 v137, v136
	v_pk_mul_f32 v[70:71], v[70:71], v[136:137]
	v_pk_mul_f32 v[72:73], v[72:73], v[136:137]
	v_pk_mul_f32 v[74:75], v[74:75], v[136:137]
	v_pk_mul_f32 v[76:77], v[76:77], v[136:137]
	v_pk_mul_f32 v[78:79], v[78:79], v[136:137]
	v_pk_mul_f32 v[80:81], v[80:81], v[136:137]
	v_pk_mul_f32 v[82:83], v[82:83], v[136:137]
	v_pk_mul_f32 v[84:85], v[84:85], v[136:137]
	v_pk_mul_f32 v[86:87], v[86:87], v[136:137]
	v_pk_mul_f32 v[88:89], v[88:89], v[136:137]
	v_pk_mul_f32 v[90:91], v[90:91], v[136:137]
	v_pk_mul_f32 v[92:93], v[92:93], v[136:137]
	v_pk_mul_f32 v[94:95], v[94:95], v[136:137]
	v_pk_mul_f32 v[96:97], v[96:97], v[136:137]
	v_pk_mul_f32 v[98:99], v[98:99], v[136:137]
	v_pk_mul_f32 v[100:101], v[100:101], v[136:137]
	v_pk_fma_f32 v[70:71], v[70:71], v[6:7], v[38:39]
	v_pk_fma_f32 v[72:73], v[72:73], v[8:9], v[40:41]
	v_pk_fma_f32 v[74:75], v[74:75], v[10:11], v[42:43]
	v_pk_fma_f32 v[76:77], v[76:77], v[12:13], v[44:45]
	v_pk_fma_f32 v[78:79], v[78:79], v[14:15], v[46:47]
	v_pk_fma_f32 v[80:81], v[80:81], v[16:17], v[48:49]
	v_pk_fma_f32 v[82:83], v[82:83], v[18:19], v[50:51]
	v_pk_fma_f32 v[84:85], v[84:85], v[20:21], v[52:53]
	v_pk_fma_f32 v[86:87], v[86:87], v[22:23], v[54:55]
	v_pk_fma_f32 v[88:89], v[88:89], v[24:25], v[56:57]
	v_pk_fma_f32 v[90:91], v[90:91], v[26:27], v[58:59]
	v_pk_fma_f32 v[92:93], v[92:93], v[28:29], v[60:61]
	v_pk_fma_f32 v[94:95], v[94:95], v[30:31], v[62:63]
	v_pk_fma_f32 v[96:97], v[96:97], v[32:33], v[64:65]
	v_pk_fma_f32 v[98:99], v[98:99], v[34:35], v[66:67]
	v_pk_fma_f32 v[100:101], v[100:101], v[36:37], v[68:69]
	v_cvt_pk_bf16_f32 v70, v70, v71
	v_cvt_pk_bf16_f32 v71, v72, v73
	v_cvt_pk_bf16_f32 v72, v74, v75
	v_cvt_pk_bf16_f32 v73, v76, v77
	v_cvt_pk_bf16_f32 v78, v78, v79
	v_cvt_pk_bf16_f32 v79, v80, v81
	v_cvt_pk_bf16_f32 v80, v82, v83
	v_cvt_pk_bf16_f32 v81, v84, v85
	v_cvt_pk_bf16_f32 v86, v86, v87
	v_cvt_pk_bf16_f32 v87, v88, v89
	v_cvt_pk_bf16_f32 v88, v90, v91
	v_cvt_pk_bf16_f32 v89, v92, v93
	v_cvt_pk_bf16_f32 v94, v94, v95
	v_cvt_pk_bf16_f32 v95, v96, v97
	v_cvt_pk_bf16_f32 v96, v98, v99
	v_cvt_pk_bf16_f32 v97, v100, v101
	s_lshl_b32 s16, s12, 12
	s_add_u32 s52, s42, s16
	s_addc_u32 s53, s43, 0
	global_store_dwordx4 v3, v[70:73], s[52:53]
	global_store_dwordx4 v3, v[78:81], s[52:53] offset:1024
	global_store_dwordx4 v3, v[86:89], s[52:53] offset:2048
	global_store_dwordx4 v3, v[94:97], s[52:53] offset:3072
	s_add_u32 s12, s12, 1
	s_cmp_ge_u32 s12, s13
	s_cbranch_scc1 .Lpq_end
	s_branch .Lpq_loop
.Lpq_end:
	s_mov_b64 s[6:7], -1
.LBB0_782:
	v_readlane_b32 s4, v255, 36
	v_readlane_b32 s8, v252, 0
	s_add_i32 s5, s4, 9
	v_readlane_b32 s9, v252, 1
	s_cmp_ge_i32 s5, s9
	v_readlane_b32 s10, v252, 2
	v_readlane_b32 s11, v252, 3
	s_cbranch_scc1 .LBB0_834
	s_waitcnt vmcnt(0)
	s_waitcnt lgkmcnt(0)
	s_barrier
	s_mov_b64 s[6:7], exec
	v_readlane_b32 s8, v254, 52
	v_readlane_b32 s9, v254, 53
	s_and_b64 s[8:9], s[6:7], s[8:9]
	s_mov_b64 exec, s[8:9]
	s_cbranch_execz .LBB0_833
	v_readlane_b32 s8, v252, 42
	s_waitcnt vmcnt(0) expcnt(0) lgkmcnt(0)
	s_nop 0
	v_mov_b32_e32 v2, s8
	ds_read_b32 v5, v2
	ds_read_b32 v2, v2 offset:4
	s_waitcnt lgkmcnt(1)
	v_cmp_ne_u32_e32 vcc, 0, v5
	s_cbranch_vccnz .LBB0_801
	v_readlane_b32 s10, v252, 4
	v_readlane_b32 s11, v252, 5
	s_load_dwordx2 s[8:9], s[10:11], 0x4
	s_mov_b32 s15, 1
	s_waitcnt lgkmcnt(0)
	s_mul_i32 s14, s8, s82
	s_mul_i32 s14, s14, s9
	s_branch .LBB0_787
